# v71 + peeled first iteration of the gates and out loops waits vmcnt(16) at its first two load segments (does not retire the previous tile's 8 epilogue stores there)
# baseline (speedup 1.0000x reference)
; #define PG8_STAGE(bufoff, gbase, voff) do { _Pragma("unroll") for (int _i = 0; _i < 2; ++_i) \
;         __builtin_amdgcn_global_load_lds((const unsigned*)((const char*)(gbase) + (voff)[_i]), (PG8_LAS unsigned*)(lds + (bufoff) + ldsw + _i * 8192), 16, 0, 0); } while (0)
; #define PG8_WAIT_V(n) asm volatile("s_waitcnt vmcnt(" #n ")" ::: "memory")
; #define PG8_BAR __builtin_amdgcn_s_barrier()
; template <class Epi, class Sched, bool ALIGN_EPI = true, bool F8 = false>
; __device__ __forceinline__ void gemm_phase(PG8_LAS unsigned char* lds, const Sched& S, const Epi& E) {
;     ...
;     PG8_STAGE(PG8_SB(0, 0), cB, voffB[0]); PG8_STAGE(PG8_SB(0, 1), cB, voffB[1]); PG8_STAGE(PG8_SA(0, 0), cA, voffA[0]); PG8_STAGE(PG8_SA(0, 1), cA, voffA[1]);
;     if (wr == 1) PG8_BAR;
;     PG8_WAIT_V(2); PG8_BAR;
;     PG8_STAGE(PG8_SB(1, 0), cB + kstepB, voffB[0]); PG8_STAGE(PG8_SA(1, 0), cA + kstep, voffA[0]); PG8_STAGE(PG8_SB(1, 1), cB + kstepB, voffB[1]);
;     PG8_WAIT_V(6); PG8_BAR;
.LBB0_418:
	s_add_u32 s53, s13, 0x4000000
	s_addc_u32 s59, s14, 0
	s_and_b32 s17, s15, 3
	s_lshl_b32 s13, s1, 13
	s_add_u32 s14, s26, 0x8000
	s_addc_u32 s15, s27, 0
	s_add_i32 m0, s48, 0x18000
	v_lshl_add_u64 v[2:3], s[14:15], 0, v[164:165]
	s_waitcnt vmcnt(2)
	s_barrier
	global_load_lds_dwordx4 v[2:3], off
	s_add_i32 m0, s48, 0x1a000
	s_add_u32 s18, s24, 0x8000
	v_lshl_add_u64 v[2:3], s[14:15], 0, v[166:167]
	s_addc_u32 s19, s25, 0
	s_add_i32 s60, s48, 0x8000
	global_load_lds_dwordx4 v[2:3], off
	v_lshl_add_u64 v[2:3], s[18:19], 0, v[174:175]
	s_mov_b32 m0, s60
	s_add_i32 s61, s48, 0xa000
	global_load_lds_dwordx4 v[2:3], off
	v_lshl_add_u64 v[2:3], s[18:19], 0, v[176:177]
	s_mov_b32 m0, s61
	v_lshlrev_b32_e32 v4, 7, v199
	global_load_lds_dwordx4 v[2:3], off
	s_add_i32 m0, s48, 0x1c000
	v_lshlrev_b32_e32 v3, 2, v163
	global_load_lds_dwordx4 v168, s[14:15]
	s_add_i32 m0, s48, 0x1e000
	v_lshl_or_b32 v2, v163, 6, v162
	global_load_lds_dwordx4 v172, s[14:15]
	v_and_b32_e32 v3, 32, v3
	v_bitop3_b32 v2, v2, s13, v3 bitop3:0xde
	v_and_b32_e32 v3, 0x3800, v200
	v_or3_b32 v3, v197, v3, v4
	v_add3_u32 v182, v3, v198, s16
	v_and_b32_e32 v3, 0x1800, v196
	s_waitcnt vmcnt(0)
	s_cmpk_lt_u32 s12, 0x100
	v_or3_b32 v3, v197, v3, v4
	v_lshl_or_b32 v191, s17, 12, v201
	s_cselect_b64 s[12:13], -1, 0
	v_add_u32_e32 v3, v3, v198
	s_add_i32 s65, 0, 0x10000
	s_add_i32 s66, 0, 0x14000
	v_mov_b32_e32 v179, v165
	v_mov_b32_e32 v181, v165
	s_sext_i32_i8 s73, s0
	v_mov_b32_e32 v169, v165
	v_mov_b32_e32 v173, v165
	v_lshl_or_b32 v190, s1, 6, v163
	s_mov_b32 s62, 0x18000
	s_mov_b32 s63, 0x8000
	s_lshl_b32 s14, s17, 6
	s_mov_b32 s15, s9
	v_mov_b32_e32 v163, v165
	s_ashr_i32 s64, s33, 31
	v_mov_b32_e32 v183, v165
	v_or_b32_e32 v184, 0x4000, v3
	v_mov_b32_e32 v185, v165
	v_mov_b64_e32 v[186:187], 0x800
	v_mov_b64_e32 v[188:189], 0x7ff
	v_add_u32_e32 v192, s65, v191
	v_add_u32_e32 v193, s66, v191
	v_add_u32_e32 v194, 0, v2
	v_mov_b32_e32 v195, 0x7f7f7f7f
	v_mov_b32_e32 v196, 0x4b000000
	s_mov_b32 s67, 0xc0c0400
	s_mov_b32 s68, 0x5040100
	s_mov_b32 s69, 0x40000
	s_mov_b32 s70, 0x48000
	s_mov_b32 s71, 0x50000
	s_mov_b32 s72, 0
	s_mov_b64 s[20:21], s[24:25]
	s_mov_b64 s[22:23], s[26:27]
	s_barrier
	s_branch .LBB0_421

; #define PG8_STAGE(bufoff, gbase, voff) do { _Pragma("unroll") for (int _i = 0; _i < 2; ++_i) \
;         __builtin_amdgcn_global_load_lds((const unsigned*)((const char*)(gbase) + (voff)[_i]), (PG8_LAS unsigned*)(lds + (bufoff) + ldsw + _i * 8192), 16, 0, 0); } while (0)
; #define PG8_WAIT_V(n) asm volatile("s_waitcnt vmcnt(" #n ")" ::: "memory")
; #define PG8_WAIT_L(n) asm volatile("s_waitcnt lgkmcnt(" #n ")" ::: "memory")
; #define PG8_BAR __builtin_amdgcn_s_barrier()
; #define PG8_SCHED __builtin_amdgcn_sched_barrier(0)
; template <class Epi, class Sched, bool ALIGN_EPI = true, bool F8 = false>
; __device__ __forceinline__ void gemm_phase(PG8_LAS unsigned char* lds, const Sched& S, const Epi& E) {
;     ...
;             PG8_LDB(B0, 0, 0); PG8_LDB(B1, 0, 1); PG8_SCHED; PG8_LDA(At, 0, 0); PG8_STAGE(PG8_SA(1, 1), a1, voffA[1]);
;             PG8_WAIT_V(8); PG8_WAIT_L(0); PG8_BAR; PG8_MMA(0, 0, At, B0); PG8_MMA(0, 1, At, B1); PG8_BAR; PG8_SCHED;
;             PG8_LDA(At, 0, 1); PG8_STAGE(PG8_SB(0, 0), b2, voffB[0]); PG8_STAGE(PG8_SB(0, 1), b2, voffB[1]); PG8_STAGE(PG8_SA(0, 0), a2, vA2[0]);
;             PG8_WAIT_V(8); PG8_WAIT_L(0); PG8_BAR; PG8_MMA(1, 0, At, B0); PG8_MMA(1, 1, At, B1); PG8_BAR; PG8_SCHED;
.Lpk0_428:
	ds_read_b128 v[18:21], v192
	ds_read_b128 v[22:25], v192 offset:1024
	ds_read_b128 v[26:29], v192 offset:2048
	ds_read_b128 v[30:33], v192 offset:3072
	ds_read_b128 v[2:5], v193
	ds_read_b128 v[6:9], v193 offset:1024
	ds_read_b128 v[10:13], v193 offset:2048
	ds_read_b128 v[14:17], v193 offset:3072
	s_add_u32 s26, s24, 0x8000
	s_addc_u32 s27, s25, 0
	s_cmp_eq_u32 s74, 12
	s_cselect_b32 s30, s20, s26
	s_cselect_b32 s31, s21, s27
	s_cselect_b32 s28, s22, s17
	s_cselect_b32 s29, s23, s19
	s_add_u32 s26, s30, 0x8000
	s_addc_u32 s27, s31, 0
	v_lshl_add_u64 v[230:231], s[24:25], 0, v[184:185]
	s_add_i32 m0, s48, 0xc000
	ds_read_b128 v[198:201], v194
	ds_read_b128 v[202:205], v194 offset:1024
	ds_read_b128 v[206:209], v194 offset:2048
	ds_read_b128 v[210:213], v194 offset:3072
	ds_read_b128 v[214:217], v194 offset:4096
	ds_read_b128 v[218:221], v194 offset:5120
	ds_read_b128 v[222:225], v194 offset:6144
	ds_read_b128 v[226:229], v194 offset:7168
	global_load_lds_dwordx4 v[230:231], off
	v_lshl_add_u64 v[230:231], s[24:25], 0, v[182:183]
	s_add_i32 m0, s48, 0xe000
	s_nop 0
	global_load_lds_dwordx4 v[230:231], off
	s_waitcnt vmcnt(16)
	s_waitcnt lgkmcnt(0)
	s_setprio 1
	v_mfma_scale_f32_16x16x128_f8f6f4 v[158:161], v[18:25], v[198:205], 0, v195, v195 op_sel_hi:[0,0,0]
	v_mfma_scale_f32_16x16x128_f8f6f4 v[154:157], v[26:33], v[198:205], 0, v195, v195 op_sel_hi:[0,0,0]
	v_mfma_scale_f32_16x16x128_f8f6f4 v[142:145], v[18:25], v[206:213], 0, v195, v195 op_sel_hi:[0,0,0]
	v_mfma_scale_f32_16x16x128_f8f6f4 v[138:141], v[26:33], v[206:213], 0, v195, v195 op_sel_hi:[0,0,0]
	v_mfma_scale_f32_16x16x128_f8f6f4 v[126:129], v[18:25], v[214:221], 0, v195, v195 op_sel_hi:[0,0,0]
	v_mfma_scale_f32_16x16x128_f8f6f4 v[122:125], v[26:33], v[214:221], 0, v195, v195 op_sel_hi:[0,0,0]
	v_mfma_scale_f32_16x16x128_f8f6f4 v[110:113], v[18:25], v[222:229], 0, v195, v195 op_sel_hi:[0,0,0]
	v_mfma_scale_f32_16x16x128_f8f6f4 v[106:109], v[26:33], v[222:229], 0, v195, v195 op_sel_hi:[0,0,0]
	s_nop 3
	s_setprio 0
	s_setprio 1
	v_mfma_scale_f32_16x16x128_f8f6f4 v[150:153], v[2:9], v[198:205], 0, v195, v195 op_sel_hi:[0,0,0]
	v_mfma_scale_f32_16x16x128_f8f6f4 v[146:149], v[10:17], v[198:205], 0, v195, v195 op_sel_hi:[0,0,0]
	v_mfma_scale_f32_16x16x128_f8f6f4 v[134:137], v[2:9], v[206:213], 0, v195, v195 op_sel_hi:[0,0,0]
	v_mfma_scale_f32_16x16x128_f8f6f4 v[130:133], v[10:17], v[206:213], 0, v195, v195 op_sel_hi:[0,0,0]
	v_mfma_scale_f32_16x16x128_f8f6f4 v[118:121], v[2:9], v[214:221], 0, v195, v195 op_sel_hi:[0,0,0]
	v_mfma_scale_f32_16x16x128_f8f6f4 v[114:117], v[10:17], v[214:221], 0, v195, v195 op_sel_hi:[0,0,0]
	v_mfma_scale_f32_16x16x128_f8f6f4 v[102:105], v[2:9], v[222:229], 0, v195, v195 op_sel_hi:[0,0,0]
	v_mfma_scale_f32_16x16x128_f8f6f4 v[98:101], v[10:17], v[222:229], 0, v195, v195 op_sel_hi:[0,0,0]
	s_setprio 0
	s_barrier
	s_add_i32 s75, s65, s47
	v_lshl_add_u64 v[230:231], s[28:29], 0, v[164:165]
	s_mov_b32 m0, s75
	ds_read_b128 v[198:201], v194 offset:16384
	ds_read_b128 v[202:205], v194 offset:17408
	ds_read_b128 v[206:209], v194 offset:18432
	ds_read_b128 v[210:213], v194 offset:19456
	ds_read_b128 v[214:217], v194 offset:20480
	ds_read_b128 v[218:221], v194 offset:21504
	ds_read_b128 v[222:225], v194 offset:22528
	ds_read_b128 v[226:229], v194 offset:23552
	global_load_lds_dwordx4 v[230:231], off
	v_lshl_add_u64 v[232:233], s[28:29], 0, v[166:167]
	s_add_i32 m0, s75, 0x2000
	s_add_i32 s75, s66, s47
	global_load_lds_dwordx4 v[232:233], off
	v_lshl_add_u64 v[230:231], v[230:231], 0, s[4:5]
	s_mov_b32 m0, s75
	s_nop 0
	global_load_lds_dwordx4 v[230:231], off
	v_lshl_add_u64 v[230:231], v[232:233], 0, s[4:5]
	s_add_i32 m0, s75, 0x2000
	s_nop 0
	global_load_lds_dwordx4 v[230:231], off
	v_lshl_add_u64 v[230:231], s[30:31], 0, v[174:175]
	s_mov_b32 m0, s48
	s_nop 0
	global_load_lds_dwordx4 v[230:231], off
	v_lshl_add_u64 v[230:231], s[30:31], 0, v[176:177]
	s_mov_b32 m0, s49
	s_nop 0
	global_load_lds_dwordx4 v[230:231], off
	s_waitcnt vmcnt(16)
	s_waitcnt lgkmcnt(0)
	s_setprio 1
	v_mfma_scale_f32_16x16x128_f8f6f4 v[94:97], v[18:25], v[198:205], 0, v195, v195 op_sel_hi:[0,0,0]
	v_mfma_scale_f32_16x16x128_f8f6f4 v[90:93], v[26:33], v[198:205], 0, v195, v195 op_sel_hi:[0,0,0]
	v_mfma_scale_f32_16x16x128_f8f6f4 v[78:81], v[18:25], v[206:213], 0, v195, v195 op_sel_hi:[0,0,0]
	v_mfma_scale_f32_16x16x128_f8f6f4 v[74:77], v[26:33], v[206:213], 0, v195, v195 op_sel_hi:[0,0,0]
	v_mfma_scale_f32_16x16x128_f8f6f4 v[62:65], v[18:25], v[214:221], 0, v195, v195 op_sel_hi:[0,0,0]
	v_mfma_scale_f32_16x16x128_f8f6f4 v[58:61], v[26:33], v[214:221], 0, v195, v195 op_sel_hi:[0,0,0]
	v_mfma_scale_f32_16x16x128_f8f6f4 v[46:49], v[18:25], v[222:229], 0, v195, v195 op_sel_hi:[0,0,0]
	v_mfma_scale_f32_16x16x128_f8f6f4 v[42:45], v[26:33], v[222:229], 0, v195, v195 op_sel_hi:[0,0,0]
	s_nop 3
	s_setprio 0
	s_setprio 1
	v_mfma_scale_f32_16x16x128_f8f6f4 v[86:89], v[2:9], v[198:205], 0, v195, v195 op_sel_hi:[0,0,0]
	v_mfma_scale_f32_16x16x128_f8f6f4 v[82:85], v[10:17], v[198:205], 0, v195, v195 op_sel_hi:[0,0,0]
	v_mfma_scale_f32_16x16x128_f8f6f4 v[70:73], v[2:9], v[206:213], 0, v195, v195 op_sel_hi:[0,0,0]
	v_mfma_scale_f32_16x16x128_f8f6f4 v[66:69], v[10:17], v[206:213], 0, v195, v195 op_sel_hi:[0,0,0]
	v_mfma_scale_f32_16x16x128_f8f6f4 v[54:57], v[2:9], v[214:221], 0, v195, v195 op_sel_hi:[0,0,0]
	v_mfma_scale_f32_16x16x128_f8f6f4 v[50:53], v[10:17], v[214:221], 0, v195, v195 op_sel_hi:[0,0,0]
	v_mfma_scale_f32_16x16x128_f8f6f4 v[38:41], v[2:9], v[222:229], 0, v195, v195 op_sel_hi:[0,0,0]
	v_mfma_scale_f32_16x16x128_f8f6f4 v[34:37], v[10:17], v[222:229], 0, v195, v195 op_sel_hi:[0,0,0]
	s_setprio 0
	s_barrier
; #define PG8_STAGE(bufoff, gbase, voff) do { _Pragma("unroll") for (int _i = 0; _i < 2; ++_i) \
;         __builtin_amdgcn_global_load_lds((const unsigned*)((const char*)(gbase) + (voff)[_i]), (PG8_LAS unsigned*)(lds + (bufoff) + ldsw + _i * 8192), 16, 0, 0); } while (0)
; #define PG8_WAIT_V(n) asm volatile("s_waitcnt vmcnt(" #n ")" ::: "memory")
; #define PG8_WAIT_L(n) asm volatile("s_waitcnt lgkmcnt(" #n ")" ::: "memory")
; #define PG8_BAR __builtin_amdgcn_s_barrier()
; #define PG8_SCHED __builtin_amdgcn_sched_barrier(0)
; template <class Epi, class Sched, bool ALIGN_EPI = true, bool F8 = false>
; __device__ __forceinline__ void gemm_phase(PG8_LAS unsigned char* lds, const Sched& S, const Epi& E) {
;     ...
;             PG8_LDB(B0, 1, 0); PG8_LDB(B1, 1, 1); PG8_SCHED; PG8_LDA(At, 1, 0); PG8_STAGE(PG8_SA(0, 1), a2, vA2[1]);
;             PG8_WAIT_V(8); PG8_WAIT_L(0); PG8_BAR; PG8_MMA(0, 0, At, B0); PG8_MMA(0, 1, At, B1); PG8_BAR; PG8_SCHED;
;             PG8_LDA(At, 1, 1); PG8_STAGE(PG8_SB(1, 0), b3, voffB[0]); PG8_STAGE(PG8_SB(1, 1), b3, voffB[1]); PG8_STAGE(PG8_SA(1, 0), a3, vA2[0]);
;             PG8_WAIT_V(8); PG8_WAIT_L(0); PG8_BAR; PG8_MMA(1, 0, At, B0); PG8_MMA(1, 1, At, B1); PG8_BAR; PG8_SCHED;
	s_add_i32 s75, 0, 0x18000
	s_add_i32 s76, 0, 0x1c000
	v_add_u32_e32 v14, s75, v191
	v_add_u32_e32 v30, s76, v191
	ds_read_b128 v[2:5], v14
	ds_read_b128 v[6:9], v14 offset:1024
	ds_read_b128 v[10:13], v14 offset:2048
	ds_read_b128 v[14:17], v14 offset:3072
	ds_read_b128 v[18:21], v30
	ds_read_b128 v[22:25], v30 offset:1024
	ds_read_b128 v[26:29], v30 offset:2048
	ds_read_b128 v[30:33], v30 offset:3072
	s_mov_b32 m0, s50
	v_lshl_add_u64 v[230:231], s[30:31], 0, v[178:179]
	ds_read_b128 v[198:201], v194 offset:32768
	ds_read_b128 v[202:205], v194 offset:33792
	ds_read_b128 v[206:209], v194 offset:34816
	ds_read_b128 v[210:213], v194 offset:35840
	ds_read_b128 v[214:217], v194 offset:36864
	ds_read_b128 v[218:221], v194 offset:37888
	ds_read_b128 v[222:225], v194 offset:38912
	ds_read_b128 v[226:229], v194 offset:39936
	global_load_lds_dwordx4 v[230:231], off
	v_lshl_add_u64 v[230:231], s[30:31], 0, v[180:181]
	s_mov_b32 m0, s51
	s_nop 0
	global_load_lds_dwordx4 v[230:231], off
	s_waitcnt vmcnt(8)
	s_waitcnt lgkmcnt(0)
	s_setprio 1
	v_mfma_scale_f32_16x16x128_f8f6f4 v[158:161], v[2:9], v[198:205], v[158:161], v195, v195 op_sel_hi:[0,0,0]
	v_mfma_scale_f32_16x16x128_f8f6f4 v[154:157], v[10:17], v[198:205], v[154:157], v195, v195 op_sel_hi:[0,0,0]
	v_mfma_scale_f32_16x16x128_f8f6f4 v[142:145], v[2:9], v[206:213], v[142:145], v195, v195 op_sel_hi:[0,0,0]
	v_mfma_scale_f32_16x16x128_f8f6f4 v[138:141], v[10:17], v[206:213], v[138:141], v195, v195 op_sel_hi:[0,0,0]
	v_mfma_scale_f32_16x16x128_f8f6f4 v[126:129], v[2:9], v[214:221], v[126:129], v195, v195 op_sel_hi:[0,0,0]
	v_mfma_scale_f32_16x16x128_f8f6f4 v[122:125], v[10:17], v[214:221], v[122:125], v195, v195 op_sel_hi:[0,0,0]
	v_mfma_scale_f32_16x16x128_f8f6f4 v[110:113], v[2:9], v[222:229], v[110:113], v195, v195 op_sel_hi:[0,0,0]
	v_mfma_scale_f32_16x16x128_f8f6f4 v[106:109], v[10:17], v[222:229], v[106:109], v195, v195 op_sel_hi:[0,0,0]
	s_nop 3
	s_setprio 0
	s_setprio 1
	v_mfma_scale_f32_16x16x128_f8f6f4 v[150:153], v[18:25], v[198:205], v[150:153], v195, v195 op_sel_hi:[0,0,0]
	v_mfma_scale_f32_16x16x128_f8f6f4 v[146:149], v[26:33], v[198:205], v[146:149], v195, v195 op_sel_hi:[0,0,0]
	v_mfma_scale_f32_16x16x128_f8f6f4 v[134:137], v[18:25], v[206:213], v[134:137], v195, v195 op_sel_hi:[0,0,0]
	v_mfma_scale_f32_16x16x128_f8f6f4 v[130:133], v[26:33], v[206:213], v[130:133], v195, v195 op_sel_hi:[0,0,0]
	v_mfma_scale_f32_16x16x128_f8f6f4 v[118:121], v[18:25], v[214:221], v[118:121], v195, v195 op_sel_hi:[0,0,0]
	v_mfma_scale_f32_16x16x128_f8f6f4 v[114:117], v[26:33], v[214:221], v[114:117], v195, v195 op_sel_hi:[0,0,0]
	v_mfma_scale_f32_16x16x128_f8f6f4 v[102:105], v[18:25], v[222:229], v[102:105], v195, v195 op_sel_hi:[0,0,0]
	v_mfma_scale_f32_16x16x128_f8f6f4 v[98:101], v[26:33], v[222:229], v[98:101], v195, v195 op_sel_hi:[0,0,0]
	s_setprio 0
	s_barrier
	s_add_u32 s28, s28, 0x8000
	s_addc_u32 s29, s29, 0
	s_add_i32 s30, s75, s47
	v_lshl_add_u64 v[230:231], s[28:29], 0, v[164:165]
	s_mov_b32 m0, s30
	ds_read_b128 v[198:201], v194 offset:49152
	ds_read_b128 v[202:205], v194 offset:50176
	ds_read_b128 v[206:209], v194 offset:51200
	ds_read_b128 v[210:213], v194 offset:52224
	ds_read_b128 v[214:217], v194 offset:53248
	ds_read_b128 v[218:221], v194 offset:54272
	ds_read_b128 v[222:225], v194 offset:55296
	ds_read_b128 v[226:229], v194 offset:56320
	global_load_lds_dwordx4 v[230:231], off
	v_lshl_add_u64 v[230:231], s[28:29], 0, v[166:167]
	s_add_i32 m0, s30, 0x2000
	s_add_i32 s30, s76, s47
	global_load_lds_dwordx4 v[230:231], off
	v_lshl_add_u64 v[230:231], s[28:29], 0, v[168:169]
	s_mov_b32 m0, s30
	s_nop 0
	global_load_lds_dwordx4 v[230:231], off
	v_lshl_add_u64 v[230:231], s[28:29], 0, v[172:173]
	s_add_i32 m0, s30, 0x2000
	s_nop 0
	global_load_lds_dwordx4 v[230:231], off
	v_lshl_add_u64 v[230:231], s[26:27], 0, v[174:175]
	s_mov_b32 m0, s60
	s_nop 0
	global_load_lds_dwordx4 v[230:231], off
	v_lshl_add_u64 v[230:231], s[26:27], 0, v[176:177]
	s_mov_b32 m0, s61
	s_nop 0
	global_load_lds_dwordx4 v[230:231], off
	s_waitcnt vmcnt(8)
	s_waitcnt lgkmcnt(0)
	s_setprio 1
	v_mfma_scale_f32_16x16x128_f8f6f4 v[94:97], v[2:9], v[198:205], v[94:97], v195, v195 op_sel_hi:[0,0,0]
	v_mfma_scale_f32_16x16x128_f8f6f4 v[90:93], v[10:17], v[198:205], v[90:93], v195, v195 op_sel_hi:[0,0,0]
	v_mfma_scale_f32_16x16x128_f8f6f4 v[78:81], v[2:9], v[206:213], v[78:81], v195, v195 op_sel_hi:[0,0,0]
	v_mfma_scale_f32_16x16x128_f8f6f4 v[74:77], v[10:17], v[206:213], v[74:77], v195, v195 op_sel_hi:[0,0,0]
	v_mfma_scale_f32_16x16x128_f8f6f4 v[62:65], v[2:9], v[214:221], v[62:65], v195, v195 op_sel_hi:[0,0,0]
	v_mfma_scale_f32_16x16x128_f8f6f4 v[58:61], v[10:17], v[214:221], v[58:61], v195, v195 op_sel_hi:[0,0,0]
	v_mfma_scale_f32_16x16x128_f8f6f4 v[46:49], v[2:9], v[222:229], v[46:49], v195, v195 op_sel_hi:[0,0,0]
	v_mfma_scale_f32_16x16x128_f8f6f4 v[42:45], v[10:17], v[222:229], v[42:45], v195, v195 op_sel_hi:[0,0,0]
	s_nop 3
	s_setprio 0
	s_setprio 1
	v_mfma_scale_f32_16x16x128_f8f6f4 v[86:89], v[18:25], v[198:205], v[86:89], v195, v195 op_sel_hi:[0,0,0]
	v_mfma_scale_f32_16x16x128_f8f6f4 v[82:85], v[26:33], v[198:205], v[82:85], v195, v195 op_sel_hi:[0,0,0]
	v_mfma_scale_f32_16x16x128_f8f6f4 v[70:73], v[18:25], v[206:213], v[70:73], v195, v195 op_sel_hi:[0,0,0]
	v_mfma_scale_f32_16x16x128_f8f6f4 v[66:69], v[26:33], v[206:213], v[66:69], v195, v195 op_sel_hi:[0,0,0]
	v_mfma_scale_f32_16x16x128_f8f6f4 v[54:57], v[18:25], v[214:221], v[54:57], v195, v195 op_sel_hi:[0,0,0]
	v_mfma_scale_f32_16x16x128_f8f6f4 v[50:53], v[26:33], v[214:221], v[50:53], v195, v195 op_sel_hi:[0,0,0]
	v_mfma_scale_f32_16x16x128_f8f6f4 v[38:41], v[18:25], v[222:229], v[38:41], v195, v195 op_sel_hi:[0,0,0]
	v_mfma_scale_f32_16x16x128_f8f6f4 v[34:37], v[26:33], v[222:229], v[34:37], v195, v195 op_sel_hi:[0,0,0]
	s_setprio 0
	s_barrier
	s_add_i32 s74, s74, 2
	s_add_u32 s17, s17, 0x10000
	s_addc_u32 s19, s19, 0
	s_add_u32 s24, s24, 0x10000
	s_addc_u32 s25, s25, 0
	s_cmp_gt_u32 s74, 13
	s_cbranch_scc0 .LBB0_428
	s_branch .Lfx_11141

; #define PG8_STAGE(bufoff, gbase, voff) do { _Pragma("unroll") for (int _i = 0; _i < 2; ++_i) \
;         __builtin_amdgcn_global_load_lds((const unsigned*)((const char*)(gbase) + (voff)[_i]), (PG8_LAS unsigned*)(lds + (bufoff) + ldsw + _i * 8192), 16, 0, 0); } while (0)
; #define PG8_WAIT_V(n) asm volatile("s_waitcnt vmcnt(" #n ")" ::: "memory")
; #define PG8_WAIT_L(n) asm volatile("s_waitcnt lgkmcnt(" #n ")" ::: "memory")
; #define PG8_BAR __builtin_amdgcn_s_barrier()
; #define PG8_SCHED __builtin_amdgcn_sched_barrier(0)
; template <class Epi, class Sched, bool ALIGN_EPI = true, bool F8 = false>
; __device__ __forceinline__ void gemm_phase(PG8_LAS unsigned char* lds, const Sched& S, const Epi& E) {
;     ...
;             PG8_LDB(B0, 0, 0); PG8_LDB(B1, 0, 1); PG8_SCHED; PG8_LDA(At, 0, 0); PG8_STAGE(PG8_SA(1, 1), a1, voffA[1]);
;             PG8_WAIT_V(8); PG8_WAIT_L(0); PG8_BAR; PG8_MMA(0, 0, At, B0); PG8_MMA(0, 1, At, B1); PG8_BAR; PG8_SCHED;
;             PG8_LDA(At, 0, 1); PG8_STAGE(PG8_SB(0, 0), b2, voffB[0]); PG8_STAGE(PG8_SB(0, 1), b2, voffB[1]); PG8_STAGE(PG8_SA(0, 0), a2, vA2[0]);
;             PG8_WAIT_V(8); PG8_WAIT_L(0); PG8_BAR; PG8_MMA(1, 0, At, B0); PG8_MMA(1, 1, At, B1); PG8_BAR; PG8_SCHED;
;             PG8_LDB(B0, 1, 0); PG8_LDB(B1, 1, 1); PG8_SCHED; PG8_LDA(At, 1, 0); PG8_STAGE(PG8_SA(0, 1), a2, vA2[1]);
;             PG8_WAIT_V(8); PG8_WAIT_L(0); PG8_BAR; PG8_MMA(0, 0, At, B0); PG8_MMA(0, 1, At, B1); PG8_BAR; PG8_SCHED;
.Lh1e_11141:
.Lpk1_428:
	ds_read_b128 v[18:21], v192
	ds_read_b128 v[22:25], v192 offset:1024
	ds_read_b128 v[26:29], v192 offset:2048
	ds_read_b128 v[30:33], v192 offset:3072
	ds_read_b128 v[2:5], v193
	ds_read_b128 v[6:9], v193 offset:1024
	ds_read_b128 v[10:13], v193 offset:2048
	ds_read_b128 v[14:17], v193 offset:3072
	s_add_u32 s26, s24, 0x8000
	s_addc_u32 s27, s25, 0
	s_cmp_eq_u32 s74, 12
	s_cselect_b32 s30, s20, s26
	s_cselect_b32 s31, s21, s27
	s_cselect_b32 s28, s22, s17
	s_cselect_b32 s29, s23, s19
	s_add_u32 s26, s30, 0x8000
	s_addc_u32 s27, s31, 0
	v_lshl_add_u64 v[230:231], s[24:25], 0, v[184:185]
	s_add_i32 m0, s48, 0xc000
	ds_read_b128 v[198:201], v194
	ds_read_b128 v[202:205], v194 offset:1024
	ds_read_b128 v[206:209], v194 offset:2048
	ds_read_b128 v[210:213], v194 offset:3072
	ds_read_b128 v[214:217], v194 offset:4096
	ds_read_b128 v[218:221], v194 offset:5120
	ds_read_b128 v[222:225], v194 offset:6144
	ds_read_b128 v[226:229], v194 offset:7168
	global_load_lds_dwordx4 v[230:231], off
	v_lshl_add_u64 v[230:231], s[24:25], 0, v[182:183]
	s_add_i32 m0, s48, 0xe000
	s_nop 0
	global_load_lds_dwordx4 v[230:231], off
	s_waitcnt vmcnt(16)
	s_waitcnt lgkmcnt(0)
	s_barrier
	s_setprio 2
	v_mfma_scale_f32_16x16x128_f8f6f4 v[158:161], v[18:25], v[198:205], 0, v195, v195 op_sel_hi:[0,0,0]
	v_mfma_scale_f32_16x16x128_f8f6f4 v[154:157], v[26:33], v[198:205], 0, v195, v195 op_sel_hi:[0,0,0]
	v_mfma_scale_f32_16x16x128_f8f6f4 v[142:145], v[18:25], v[206:213], 0, v195, v195 op_sel_hi:[0,0,0]
	v_mfma_scale_f32_16x16x128_f8f6f4 v[138:141], v[26:33], v[206:213], 0, v195, v195 op_sel_hi:[0,0,0]
	v_mfma_scale_f32_16x16x128_f8f6f4 v[126:129], v[18:25], v[214:221], 0, v195, v195 op_sel_hi:[0,0,0]
	v_mfma_scale_f32_16x16x128_f8f6f4 v[122:125], v[26:33], v[214:221], 0, v195, v195 op_sel_hi:[0,0,0]
	v_mfma_scale_f32_16x16x128_f8f6f4 v[110:113], v[18:25], v[222:229], 0, v195, v195 op_sel_hi:[0,0,0]
	v_mfma_scale_f32_16x16x128_f8f6f4 v[106:109], v[26:33], v[222:229], 0, v195, v195 op_sel_hi:[0,0,0]
	s_nop 3
	s_setprio 0
	s_setprio 2
	v_mfma_scale_f32_16x16x128_f8f6f4 v[150:153], v[2:9], v[198:205], 0, v195, v195 op_sel_hi:[0,0,0]
	v_mfma_scale_f32_16x16x128_f8f6f4 v[146:149], v[10:17], v[198:205], 0, v195, v195 op_sel_hi:[0,0,0]
	v_mfma_scale_f32_16x16x128_f8f6f4 v[134:137], v[2:9], v[206:213], 0, v195, v195 op_sel_hi:[0,0,0]
	v_mfma_scale_f32_16x16x128_f8f6f4 v[130:133], v[10:17], v[206:213], 0, v195, v195 op_sel_hi:[0,0,0]
	v_mfma_scale_f32_16x16x128_f8f6f4 v[118:121], v[2:9], v[214:221], 0, v195, v195 op_sel_hi:[0,0,0]
	v_mfma_scale_f32_16x16x128_f8f6f4 v[114:117], v[10:17], v[214:221], 0, v195, v195 op_sel_hi:[0,0,0]
	v_mfma_scale_f32_16x16x128_f8f6f4 v[102:105], v[2:9], v[222:229], 0, v195, v195 op_sel_hi:[0,0,0]
	v_mfma_scale_f32_16x16x128_f8f6f4 v[98:101], v[10:17], v[222:229], 0, v195, v195 op_sel_hi:[0,0,0]
	s_setprio 0
	s_add_i32 s75, s65, s47
	v_lshl_add_u64 v[230:231], s[28:29], 0, v[164:165]
	s_mov_b32 m0, s75
	ds_read_b128 v[198:201], v194 offset:16384
	ds_read_b128 v[202:205], v194 offset:17408
	ds_read_b128 v[206:209], v194 offset:18432
	ds_read_b128 v[210:213], v194 offset:19456
	ds_read_b128 v[214:217], v194 offset:20480
	ds_read_b128 v[218:221], v194 offset:21504
	ds_read_b128 v[222:225], v194 offset:22528
	ds_read_b128 v[226:229], v194 offset:23552
	global_load_lds_dwordx4 v[230:231], off
	v_lshl_add_u64 v[232:233], s[28:29], 0, v[166:167]
	s_add_i32 m0, s75, 0x2000
	s_add_i32 s75, s66, s47
	global_load_lds_dwordx4 v[232:233], off
	v_lshl_add_u64 v[230:231], v[230:231], 0, s[4:5]
	s_mov_b32 m0, s75
	s_nop 0
	global_load_lds_dwordx4 v[230:231], off
	v_lshl_add_u64 v[230:231], v[232:233], 0, s[4:5]
	s_add_i32 m0, s75, 0x2000
	s_nop 0
	global_load_lds_dwordx4 v[230:231], off
	v_lshl_add_u64 v[230:231], s[30:31], 0, v[174:175]
	s_mov_b32 m0, s48
	s_nop 0
	global_load_lds_dwordx4 v[230:231], off
	v_lshl_add_u64 v[230:231], s[30:31], 0, v[176:177]
	s_mov_b32 m0, s49
	s_nop 0
	global_load_lds_dwordx4 v[230:231], off
	s_waitcnt vmcnt(16)
	s_waitcnt lgkmcnt(0)
	s_barrier
	s_setprio 2
	v_mfma_scale_f32_16x16x128_f8f6f4 v[94:97], v[18:25], v[198:205], 0, v195, v195 op_sel_hi:[0,0,0]
	v_mfma_scale_f32_16x16x128_f8f6f4 v[90:93], v[26:33], v[198:205], 0, v195, v195 op_sel_hi:[0,0,0]
	v_mfma_scale_f32_16x16x128_f8f6f4 v[78:81], v[18:25], v[206:213], 0, v195, v195 op_sel_hi:[0,0,0]
	v_mfma_scale_f32_16x16x128_f8f6f4 v[74:77], v[26:33], v[206:213], 0, v195, v195 op_sel_hi:[0,0,0]
	v_mfma_scale_f32_16x16x128_f8f6f4 v[62:65], v[18:25], v[214:221], 0, v195, v195 op_sel_hi:[0,0,0]
	v_mfma_scale_f32_16x16x128_f8f6f4 v[58:61], v[26:33], v[214:221], 0, v195, v195 op_sel_hi:[0,0,0]
	v_mfma_scale_f32_16x16x128_f8f6f4 v[46:49], v[18:25], v[222:229], 0, v195, v195 op_sel_hi:[0,0,0]
	v_mfma_scale_f32_16x16x128_f8f6f4 v[42:45], v[26:33], v[222:229], 0, v195, v195 op_sel_hi:[0,0,0]
	s_nop 3
	s_setprio 0
	s_setprio 2
	v_mfma_scale_f32_16x16x128_f8f6f4 v[86:89], v[2:9], v[198:205], 0, v195, v195 op_sel_hi:[0,0,0]
	v_mfma_scale_f32_16x16x128_f8f6f4 v[82:85], v[10:17], v[198:205], 0, v195, v195 op_sel_hi:[0,0,0]
	v_mfma_scale_f32_16x16x128_f8f6f4 v[70:73], v[2:9], v[206:213], 0, v195, v195 op_sel_hi:[0,0,0]
	v_mfma_scale_f32_16x16x128_f8f6f4 v[66:69], v[10:17], v[206:213], 0, v195, v195 op_sel_hi:[0,0,0]
	v_mfma_scale_f32_16x16x128_f8f6f4 v[54:57], v[2:9], v[214:221], 0, v195, v195 op_sel_hi:[0,0,0]
	v_mfma_scale_f32_16x16x128_f8f6f4 v[50:53], v[10:17], v[214:221], 0, v195, v195 op_sel_hi:[0,0,0]
	v_mfma_scale_f32_16x16x128_f8f6f4 v[38:41], v[2:9], v[222:229], 0, v195, v195 op_sel_hi:[0,0,0]
	v_mfma_scale_f32_16x16x128_f8f6f4 v[34:37], v[10:17], v[222:229], 0, v195, v195 op_sel_hi:[0,0,0]
	s_setprio 0
	s_add_i32 s75, 0, 0x18000
	s_add_i32 s76, 0, 0x1c000
	v_add_u32_e32 v14, s75, v191
	v_add_u32_e32 v30, s76, v191
	ds_read_b128 v[2:5], v14
	ds_read_b128 v[6:9], v14 offset:1024
	ds_read_b128 v[10:13], v14 offset:2048
	ds_read_b128 v[14:17], v14 offset:3072
	ds_read_b128 v[18:21], v30
	ds_read_b128 v[22:25], v30 offset:1024
	ds_read_b128 v[26:29], v30 offset:2048
	ds_read_b128 v[30:33], v30 offset:3072
	s_mov_b32 m0, s50
	v_lshl_add_u64 v[230:231], s[30:31], 0, v[178:179]
	ds_read_b128 v[198:201], v194 offset:32768
	ds_read_b128 v[202:205], v194 offset:33792
	ds_read_b128 v[206:209], v194 offset:34816
	ds_read_b128 v[210:213], v194 offset:35840
	ds_read_b128 v[214:217], v194 offset:36864
	ds_read_b128 v[218:221], v194 offset:37888
	ds_read_b128 v[222:225], v194 offset:38912
	ds_read_b128 v[226:229], v194 offset:39936
	global_load_lds_dwordx4 v[230:231], off
	v_lshl_add_u64 v[230:231], s[30:31], 0, v[180:181]
	s_mov_b32 m0, s51
	s_nop 0
	global_load_lds_dwordx4 v[230:231], off
	s_waitcnt vmcnt(8)
	s_waitcnt lgkmcnt(0)
	s_barrier
; #define PG8_STAGE(bufoff, gbase, voff) do { _Pragma("unroll") for (int _i = 0; _i < 2; ++_i) \
;         __builtin_amdgcn_global_load_lds((const unsigned*)((const char*)(gbase) + (voff)[_i]), (PG8_LAS unsigned*)(lds + (bufoff) + ldsw + _i * 8192), 16, 0, 0); } while (0)
; #define PG8_WAIT_V(n) asm volatile("s_waitcnt vmcnt(" #n ")" ::: "memory")
; #define PG8_WAIT_L(n) asm volatile("s_waitcnt lgkmcnt(" #n ")" ::: "memory")
; #define PG8_BAR __builtin_amdgcn_s_barrier()
; #define PG8_SCHED __builtin_amdgcn_sched_barrier(0)
; template <class Epi, class Sched, bool ALIGN_EPI = true, bool F8 = false>
; __device__ __forceinline__ void gemm_phase(PG8_LAS unsigned char* lds, const Sched& S, const Epi& E) {
;     ...
;             PG8_WAIT_V(8); PG8_WAIT_L(0); PG8_BAR; PG8_MMA(0, 0, At, B0); PG8_MMA(0, 1, At, B1); PG8_BAR; PG8_SCHED;
;             PG8_LDA(At, 1, 1); PG8_STAGE(PG8_SB(1, 0), b3, voffB[0]); PG8_STAGE(PG8_SB(1, 1), b3, voffB[1]); PG8_STAGE(PG8_SA(1, 0), a3, vA2[0]);
;             PG8_WAIT_V(8); PG8_WAIT_L(0); PG8_BAR; PG8_MMA(1, 0, At, B0); PG8_MMA(1, 1, At, B1); PG8_BAR; PG8_SCHED;
	s_setprio 2
	v_mfma_scale_f32_16x16x128_f8f6f4 v[158:161], v[2:9], v[198:205], v[158:161], v195, v195 op_sel_hi:[0,0,0]
	v_mfma_scale_f32_16x16x128_f8f6f4 v[154:157], v[10:17], v[198:205], v[154:157], v195, v195 op_sel_hi:[0,0,0]
	v_mfma_scale_f32_16x16x128_f8f6f4 v[142:145], v[2:9], v[206:213], v[142:145], v195, v195 op_sel_hi:[0,0,0]
	v_mfma_scale_f32_16x16x128_f8f6f4 v[138:141], v[10:17], v[206:213], v[138:141], v195, v195 op_sel_hi:[0,0,0]
	v_mfma_scale_f32_16x16x128_f8f6f4 v[126:129], v[2:9], v[214:221], v[126:129], v195, v195 op_sel_hi:[0,0,0]
	v_mfma_scale_f32_16x16x128_f8f6f4 v[122:125], v[10:17], v[214:221], v[122:125], v195, v195 op_sel_hi:[0,0,0]
	v_mfma_scale_f32_16x16x128_f8f6f4 v[110:113], v[2:9], v[222:229], v[110:113], v195, v195 op_sel_hi:[0,0,0]
	v_mfma_scale_f32_16x16x128_f8f6f4 v[106:109], v[10:17], v[222:229], v[106:109], v195, v195 op_sel_hi:[0,0,0]
	s_nop 3
	s_setprio 0
	s_setprio 2
	v_mfma_scale_f32_16x16x128_f8f6f4 v[150:153], v[18:25], v[198:205], v[150:153], v195, v195 op_sel_hi:[0,0,0]
	v_mfma_scale_f32_16x16x128_f8f6f4 v[146:149], v[26:33], v[198:205], v[146:149], v195, v195 op_sel_hi:[0,0,0]
	v_mfma_scale_f32_16x16x128_f8f6f4 v[134:137], v[18:25], v[206:213], v[134:137], v195, v195 op_sel_hi:[0,0,0]
	v_mfma_scale_f32_16x16x128_f8f6f4 v[130:133], v[26:33], v[206:213], v[130:133], v195, v195 op_sel_hi:[0,0,0]
	v_mfma_scale_f32_16x16x128_f8f6f4 v[118:121], v[18:25], v[214:221], v[118:121], v195, v195 op_sel_hi:[0,0,0]
	v_mfma_scale_f32_16x16x128_f8f6f4 v[114:117], v[26:33], v[214:221], v[114:117], v195, v195 op_sel_hi:[0,0,0]
	v_mfma_scale_f32_16x16x128_f8f6f4 v[102:105], v[18:25], v[222:229], v[102:105], v195, v195 op_sel_hi:[0,0,0]
	v_mfma_scale_f32_16x16x128_f8f6f4 v[98:101], v[26:33], v[222:229], v[98:101], v195, v195 op_sel_hi:[0,0,0]
	s_setprio 0
	s_add_u32 s28, s28, 0x8000
	s_addc_u32 s29, s29, 0
	s_add_i32 s30, s75, s47
	v_lshl_add_u64 v[230:231], s[28:29], 0, v[164:165]
	s_mov_b32 m0, s30
	ds_read_b128 v[198:201], v194 offset:49152
	ds_read_b128 v[202:205], v194 offset:50176
	ds_read_b128 v[206:209], v194 offset:51200
	ds_read_b128 v[210:213], v194 offset:52224
	ds_read_b128 v[214:217], v194 offset:53248
	ds_read_b128 v[218:221], v194 offset:54272
	ds_read_b128 v[222:225], v194 offset:55296
	ds_read_b128 v[226:229], v194 offset:56320
	global_load_lds_dwordx4 v[230:231], off
	v_lshl_add_u64 v[230:231], s[28:29], 0, v[166:167]
	s_add_i32 m0, s30, 0x2000
	s_add_i32 s30, s76, s47
	global_load_lds_dwordx4 v[230:231], off
	v_lshl_add_u64 v[230:231], s[28:29], 0, v[168:169]
	s_mov_b32 m0, s30
	s_nop 0
	global_load_lds_dwordx4 v[230:231], off
	v_lshl_add_u64 v[230:231], s[28:29], 0, v[172:173]
	s_add_i32 m0, s30, 0x2000
	s_nop 0
	global_load_lds_dwordx4 v[230:231], off
	v_lshl_add_u64 v[230:231], s[26:27], 0, v[174:175]
	s_mov_b32 m0, s60
	s_nop 0
	global_load_lds_dwordx4 v[230:231], off
	v_lshl_add_u64 v[230:231], s[26:27], 0, v[176:177]
	s_mov_b32 m0, s61
	s_nop 0
	global_load_lds_dwordx4 v[230:231], off
	s_waitcnt vmcnt(8)
	s_waitcnt lgkmcnt(0)
	s_barrier
	s_setprio 2
	v_mfma_scale_f32_16x16x128_f8f6f4 v[94:97], v[2:9], v[198:205], v[94:97], v195, v195 op_sel_hi:[0,0,0]
	v_mfma_scale_f32_16x16x128_f8f6f4 v[90:93], v[10:17], v[198:205], v[90:93], v195, v195 op_sel_hi:[0,0,0]
	v_mfma_scale_f32_16x16x128_f8f6f4 v[78:81], v[2:9], v[206:213], v[78:81], v195, v195 op_sel_hi:[0,0,0]
	v_mfma_scale_f32_16x16x128_f8f6f4 v[74:77], v[10:17], v[206:213], v[74:77], v195, v195 op_sel_hi:[0,0,0]
	v_mfma_scale_f32_16x16x128_f8f6f4 v[62:65], v[2:9], v[214:221], v[62:65], v195, v195 op_sel_hi:[0,0,0]
	v_mfma_scale_f32_16x16x128_f8f6f4 v[58:61], v[10:17], v[214:221], v[58:61], v195, v195 op_sel_hi:[0,0,0]
	v_mfma_scale_f32_16x16x128_f8f6f4 v[46:49], v[2:9], v[222:229], v[46:49], v195, v195 op_sel_hi:[0,0,0]
	v_mfma_scale_f32_16x16x128_f8f6f4 v[42:45], v[10:17], v[222:229], v[42:45], v195, v195 op_sel_hi:[0,0,0]
	s_nop 3
	s_setprio 0
	s_setprio 2
	v_mfma_scale_f32_16x16x128_f8f6f4 v[86:89], v[18:25], v[198:205], v[86:89], v195, v195 op_sel_hi:[0,0,0]
	v_mfma_scale_f32_16x16x128_f8f6f4 v[82:85], v[26:33], v[198:205], v[82:85], v195, v195 op_sel_hi:[0,0,0]
	v_mfma_scale_f32_16x16x128_f8f6f4 v[70:73], v[18:25], v[206:213], v[70:73], v195, v195 op_sel_hi:[0,0,0]
	v_mfma_scale_f32_16x16x128_f8f6f4 v[66:69], v[26:33], v[206:213], v[66:69], v195, v195 op_sel_hi:[0,0,0]
	v_mfma_scale_f32_16x16x128_f8f6f4 v[54:57], v[18:25], v[214:221], v[54:57], v195, v195 op_sel_hi:[0,0,0]
	v_mfma_scale_f32_16x16x128_f8f6f4 v[50:53], v[26:33], v[214:221], v[50:53], v195, v195 op_sel_hi:[0,0,0]
	v_mfma_scale_f32_16x16x128_f8f6f4 v[38:41], v[18:25], v[222:229], v[38:41], v195, v195 op_sel_hi:[0,0,0]
	v_mfma_scale_f32_16x16x128_f8f6f4 v[34:37], v[26:33], v[222:229], v[34:37], v195, v195 op_sel_hi:[0,0,0]
	s_setprio 0
	s_add_i32 s74, s74, 2
	s_add_u32 s17, s17, 0x10000
	s_addc_u32 s19, s19, 0
	s_add_u32 s24, s24, 0x10000
	s_addc_u32 s25, s25, 0
	s_cmp_gt_u32 s74, 13
	s_cbranch_scc0 .Lh1_428
	s_branch .Lfx_11141

; #define PG8_STAGE(bufoff, gbase, voff) do { _Pragma("unroll") for (int _i = 0; _i < 2; ++_i) \
;         __builtin_amdgcn_global_load_lds((const unsigned*)((const char*)(gbase) + (voff)[_i]), (PG8_LAS unsigned*)(lds + (bufoff) + ldsw + _i * 8192), 16, 0, 0); } while (0)
; #define PG8_WAIT_V(n) asm volatile("s_waitcnt vmcnt(" #n ")" ::: "memory")
; #define PG8_BAR __builtin_amdgcn_s_barrier()
; template <class Epi, class Sched, bool ALIGN_EPI = true, bool F8 = false>
; __device__ __forceinline__ void gemm_phase(PG8_LAS unsigned char* lds, const Sched& S, const Epi& E) {
;     ...
;     PG8_STAGE(PG8_SB(0, 0), cB, voffB[0]); PG8_STAGE(PG8_SB(0, 1), cB, voffB[1]); PG8_STAGE(PG8_SA(0, 0), cA, voffA[0]); PG8_STAGE(PG8_SA(0, 1), cA, voffA[1]);
;     if (wr == 1) PG8_BAR;
;     PG8_WAIT_V(2); PG8_BAR;
;     PG8_STAGE(PG8_SB(1, 0), cB + kstepB, voffB[0]); PG8_STAGE(PG8_SA(1, 0), cA + kstep, voffA[0]); PG8_STAGE(PG8_SB(1, 1), cB + kstepB, voffB[1]);
;     PG8_WAIT_V(6); PG8_BAR;
.LBB0_901:
	s_add_u32 s10, s36, 0x1e000000
	s_addc_u32 s11, s37, 0
	s_and_b32 s15, s13, 3
	s_lshl_b32 s13, s1, 13
	s_lshl_b32 s16, s15, 12
	s_add_u32 s18, s30, 0x8000
	s_addc_u32 s19, s31, 0
	s_add_i32 m0, s27, 0x18000
	v_lshl_add_u64 v[8:9], s[18:19], 0, v[162:163]
	s_waitcnt vmcnt(2)
	s_barrier
	global_load_lds_dwordx4 v[8:9], off
	s_add_i32 m0, s27, 0x1a000
	s_add_u32 s20, s28, 0x8000
	v_lshl_add_u64 v[8:9], s[18:19], 0, v[164:165]
	s_addc_u32 s21, s29, 0
	s_add_i32 s53, s27, 0x8000
	global_load_lds_dwordx4 v[8:9], off
	v_lshl_add_u64 v[8:9], s[20:21], 0, v[166:167]
	s_mov_b32 m0, s53
	s_add_i32 s58, s27, 0xa000
	global_load_lds_dwordx4 v[8:9], off
	v_lshl_add_u64 v[8:9], s[20:21], 0, v[168:169]
	s_mov_b32 m0, s58
	v_or_b32_e32 v176, 0x400, v162
	global_load_lds_dwordx4 v[8:9], off
	s_add_i32 m0, s27, 0x1c000
	v_or_b32_e32 v178, 0x400, v164
	global_load_lds_dwordx4 v176, s[18:19]
	s_add_i32 m0, s27, 0x1e000
	s_sext_i32_i8 s64, s0
	global_load_lds_dwordx4 v178, s[18:19]
	v_and_b32_e32 v8, 15, v0
	v_lshlrev_b32_e32 v9, 2, v0
	v_lshlrev_b32_e32 v10, 6, v0
	s_movk_i32 s0, 0x3c0
	v_lshlrev_b32_e32 v5, 7, v5
	v_and_b32_e32 v2, 0x1800, v2
	v_lshl_or_b32 v188, s1, 6, v8
	v_lshl_or_b32 v8, v8, 6, v7
	v_and_b32_e32 v9, 32, v9
	v_and_or_b32 v10, v10, s0, v7
	s_waitcnt vmcnt(0)
	s_cmpk_lt_u32 s12, 0x100
	v_and_b32_e32 v6, 0x3800, v6
	v_or3_b32 v2, v3, v2, v5
	v_bitop3_b32 v8, v8, s13, v9 bitop3:0xde
	v_bitop3_b32 v189, s16, v10, v9 bitop3:0xf6
	s_cselect_b64 s[12:13], -1, 0
	v_or3_b32 v6, v3, v6, v5
	v_add_u32_e32 v2, v2, v4
	s_add_i32 s60, 0, 0x10000
	s_add_i32 s61, 0, 0x14000
	v_mov_b32_e32 v173, v163
	v_mov_b32_e32 v175, v163
	v_mov_b32_e32 v177, v163
	v_mov_b32_e32 v179, v163
	s_ashr_i32 s59, s33, 31
	v_lshl_or_b32 v190, s15, 6, v7
	v_add3_u32 v180, v6, v4, s14
	v_mov_b32_e32 v181, v163
	v_or_b32_e32 v182, 0x4000, v2
	v_mov_b32_e32 v183, v163
	v_mov_b64_e32 v[184:185], 0x400
	v_mov_b64_e32 v[186:187], 0x3ff
	v_add_u32_e32 v191, s60, v189
	v_add_u32_e32 v192, s61, v189
	v_add_u32_e32 v193, 0, v8
	v_mov_b32_e32 v194, 0x7f7f7f7f
	s_mov_b64 s[14:15], 0x504000
	s_mov_b32 s62, 0x504000
	s_mov_b32 s16, 0x3e800000
	s_mov_b32 s63, 0xc3e00000
	v_mov_b32_e32 v195, 0x43e00000
	s_mov_b64 s[22:23], s[28:29]
	s_mov_b64 s[24:25], s[30:31]
	s_barrier
	s_branch .LBB0_904

; #define PG8_STAGE(bufoff, gbase, voff) do { _Pragma("unroll") for (int _i = 0; _i < 2; ++_i) \
;         __builtin_amdgcn_global_load_lds((const unsigned*)((const char*)(gbase) + (voff)[_i]), (PG8_LAS unsigned*)(lds + (bufoff) + ldsw + _i * 8192), 16, 0, 0); } while (0)
; #define PG8_WAIT_V(n) asm volatile("s_waitcnt vmcnt(" #n ")" ::: "memory")
; #define PG8_WAIT_L(n) asm volatile("s_waitcnt lgkmcnt(" #n ")" ::: "memory")
; #define PG8_BAR __builtin_amdgcn_s_barrier()
; #define PG8_SCHED __builtin_amdgcn_sched_barrier(0)
; template <class Epi, class Sched, bool ALIGN_EPI = true, bool F8 = false>
; __device__ __forceinline__ void gemm_phase(PG8_LAS unsigned char* lds, const Sched& S, const Epi& E) {
;     ...
;             PG8_LDB(B0, 0, 0); PG8_LDB(B1, 0, 1); PG8_SCHED; PG8_LDA(At, 0, 0); PG8_STAGE(PG8_SA(1, 1), a1, voffA[1]);
;             PG8_WAIT_V(8); PG8_WAIT_L(0); PG8_BAR; PG8_MMA(0, 0, At, B0); PG8_MMA(0, 1, At, B1); PG8_BAR; PG8_SCHED;
;             PG8_LDA(At, 0, 1); PG8_STAGE(PG8_SB(0, 0), b2, voffB[0]); PG8_STAGE(PG8_SB(0, 1), b2, voffB[1]); PG8_STAGE(PG8_SA(0, 0), a2, vA2[0]);
;             PG8_WAIT_V(8); PG8_WAIT_L(0); PG8_BAR; PG8_MMA(1, 0, At, B0); PG8_MMA(1, 1, At, B1); PG8_BAR; PG8_SCHED;
.Lpk0_911:
	ds_read_b128 v[18:21], v191
	ds_read_b128 v[22:25], v191 offset:1024
	ds_read_b128 v[26:29], v191 offset:2048
	ds_read_b128 v[30:33], v191 offset:3072
	ds_read_b128 v[2:5], v192
	ds_read_b128 v[6:9], v192 offset:1024
	ds_read_b128 v[10:13], v192 offset:2048
	ds_read_b128 v[14:17], v192 offset:3072
	s_add_u32 s30, s28, 0x8000
	s_addc_u32 s31, s29, 0
	s_cmp_eq_u32 s65, 12
	s_cselect_b32 s42, s22, s30
	s_cselect_b32 s43, s23, s31
	s_cselect_b32 s40, s24, s19
	s_cselect_b32 s41, s25, s21
	s_add_u32 s30, s42, 0x8000
	s_addc_u32 s31, s43, 0
	v_lshl_add_u64 v[228:229], s[28:29], 0, v[182:183]
	s_add_i32 m0, s27, 0xc000
	ds_read_b128 v[196:199], v193
	ds_read_b128 v[200:203], v193 offset:1024
	ds_read_b128 v[204:207], v193 offset:2048
	ds_read_b128 v[208:211], v193 offset:3072
	ds_read_b128 v[212:215], v193 offset:4096
	ds_read_b128 v[216:219], v193 offset:5120
	ds_read_b128 v[220:223], v193 offset:6144
	ds_read_b128 v[224:227], v193 offset:7168
	global_load_lds_dwordx4 v[228:229], off
	v_lshl_add_u64 v[228:229], s[28:29], 0, v[180:181]
	s_add_i32 m0, s27, 0xe000
	s_nop 0
	global_load_lds_dwordx4 v[228:229], off
	s_waitcnt vmcnt(16)
	s_waitcnt lgkmcnt(0)
	s_setprio 1
	v_mfma_scale_f32_16x16x128_f8f6f4 v[158:161], v[18:25], v[196:203], 0, v194, v194 op_sel_hi:[0,0,0]
	v_mfma_scale_f32_16x16x128_f8f6f4 v[154:157], v[26:33], v[196:203], 0, v194, v194 op_sel_hi:[0,0,0]
	v_mfma_scale_f32_16x16x128_f8f6f4 v[150:153], v[18:25], v[204:211], 0, v194, v194 op_sel_hi:[0,0,0]
	v_mfma_scale_f32_16x16x128_f8f6f4 v[146:149], v[26:33], v[204:211], 0, v194, v194 op_sel_hi:[0,0,0]
	v_mfma_scale_f32_16x16x128_f8f6f4 v[130:133], v[18:25], v[212:219], 0, v194, v194 op_sel_hi:[0,0,0]
	v_mfma_scale_f32_16x16x128_f8f6f4 v[122:125], v[26:33], v[212:219], 0, v194, v194 op_sel_hi:[0,0,0]
	v_mfma_scale_f32_16x16x128_f8f6f4 v[114:117], v[18:25], v[220:227], 0, v194, v194 op_sel_hi:[0,0,0]
	v_mfma_scale_f32_16x16x128_f8f6f4 v[106:109], v[26:33], v[220:227], 0, v194, v194 op_sel_hi:[0,0,0]
	s_nop 3
	s_setprio 0
	s_setprio 1
	v_mfma_scale_f32_16x16x128_f8f6f4 v[142:145], v[2:9], v[196:203], 0, v194, v194 op_sel_hi:[0,0,0]
	v_mfma_scale_f32_16x16x128_f8f6f4 v[138:141], v[10:17], v[196:203], 0, v194, v194 op_sel_hi:[0,0,0]
	v_mfma_scale_f32_16x16x128_f8f6f4 v[134:137], v[2:9], v[204:211], 0, v194, v194 op_sel_hi:[0,0,0]
	v_mfma_scale_f32_16x16x128_f8f6f4 v[126:129], v[10:17], v[204:211], 0, v194, v194 op_sel_hi:[0,0,0]
	v_mfma_scale_f32_16x16x128_f8f6f4 v[118:121], v[2:9], v[212:219], 0, v194, v194 op_sel_hi:[0,0,0]
	v_mfma_scale_f32_16x16x128_f8f6f4 v[110:113], v[10:17], v[212:219], 0, v194, v194 op_sel_hi:[0,0,0]
	v_mfma_scale_f32_16x16x128_f8f6f4 v[102:105], v[2:9], v[220:227], 0, v194, v194 op_sel_hi:[0,0,0]
	v_mfma_scale_f32_16x16x128_f8f6f4 v[98:101], v[10:17], v[220:227], 0, v194, v194 op_sel_hi:[0,0,0]
	s_setprio 0
	s_barrier
	s_add_i32 s66, s60, s48
	v_lshl_add_u64 v[228:229], s[40:41], 0, v[162:163]
	s_mov_b32 m0, s66
	ds_read_b128 v[196:199], v193 offset:16384
	ds_read_b128 v[200:203], v193 offset:17408
	ds_read_b128 v[204:207], v193 offset:18432
	ds_read_b128 v[208:211], v193 offset:19456
	ds_read_b128 v[212:215], v193 offset:20480
	ds_read_b128 v[216:219], v193 offset:21504
	ds_read_b128 v[220:223], v193 offset:22528
	ds_read_b128 v[224:227], v193 offset:23552
	global_load_lds_dwordx4 v[228:229], off
	v_lshl_add_u64 v[230:231], s[40:41], 0, v[164:165]
	s_add_i32 m0, s66, 0x2000
	s_add_i32 s66, s61, s48
	global_load_lds_dwordx4 v[230:231], off
	v_lshl_add_u64 v[228:229], v[228:229], 0, s[6:7]
	s_mov_b32 m0, s66
	s_nop 0
	global_load_lds_dwordx4 v[228:229], off
	v_lshl_add_u64 v[228:229], v[230:231], 0, s[6:7]
	s_add_i32 m0, s66, 0x2000
	s_nop 0
	global_load_lds_dwordx4 v[228:229], off
	v_lshl_add_u64 v[228:229], s[42:43], 0, v[166:167]
	s_mov_b32 m0, s27
	s_nop 0
	global_load_lds_dwordx4 v[228:229], off
	v_lshl_add_u64 v[228:229], s[42:43], 0, v[168:169]
	s_mov_b32 m0, s49
	s_nop 0
	global_load_lds_dwordx4 v[228:229], off
	s_waitcnt vmcnt(16)
	s_waitcnt lgkmcnt(0)
	s_setprio 1
	v_mfma_scale_f32_16x16x128_f8f6f4 v[94:97], v[18:25], v[196:203], 0, v194, v194 op_sel_hi:[0,0,0]
	v_mfma_scale_f32_16x16x128_f8f6f4 v[90:93], v[26:33], v[196:203], 0, v194, v194 op_sel_hi:[0,0,0]
	v_mfma_scale_f32_16x16x128_f8f6f4 v[82:85], v[18:25], v[204:211], 0, v194, v194 op_sel_hi:[0,0,0]
	v_mfma_scale_f32_16x16x128_f8f6f4 v[74:77], v[26:33], v[204:211], 0, v194, v194 op_sel_hi:[0,0,0]
	v_mfma_scale_f32_16x16x128_f8f6f4 v[66:69], v[18:25], v[212:219], 0, v194, v194 op_sel_hi:[0,0,0]
	v_mfma_scale_f32_16x16x128_f8f6f4 v[58:61], v[26:33], v[212:219], 0, v194, v194 op_sel_hi:[0,0,0]
	v_mfma_scale_f32_16x16x128_f8f6f4 v[50:53], v[18:25], v[220:227], 0, v194, v194 op_sel_hi:[0,0,0]
	v_mfma_scale_f32_16x16x128_f8f6f4 v[42:45], v[26:33], v[220:227], 0, v194, v194 op_sel_hi:[0,0,0]
	s_nop 3
	s_setprio 0
	s_setprio 1
	v_mfma_scale_f32_16x16x128_f8f6f4 v[86:89], v[2:9], v[196:203], 0, v194, v194 op_sel_hi:[0,0,0]
	v_mfma_scale_f32_16x16x128_f8f6f4 v[78:81], v[10:17], v[196:203], 0, v194, v194 op_sel_hi:[0,0,0]
	v_mfma_scale_f32_16x16x128_f8f6f4 v[70:73], v[2:9], v[204:211], 0, v194, v194 op_sel_hi:[0,0,0]
	v_mfma_scale_f32_16x16x128_f8f6f4 v[62:65], v[10:17], v[204:211], 0, v194, v194 op_sel_hi:[0,0,0]
	v_mfma_scale_f32_16x16x128_f8f6f4 v[54:57], v[2:9], v[212:219], 0, v194, v194 op_sel_hi:[0,0,0]
	v_mfma_scale_f32_16x16x128_f8f6f4 v[46:49], v[10:17], v[212:219], 0, v194, v194 op_sel_hi:[0,0,0]
	v_mfma_scale_f32_16x16x128_f8f6f4 v[38:41], v[2:9], v[220:227], 0, v194, v194 op_sel_hi:[0,0,0]
	v_mfma_scale_f32_16x16x128_f8f6f4 v[34:37], v[10:17], v[220:227], 0, v194, v194 op_sel_hi:[0,0,0]
	s_setprio 0
	s_barrier
; #define PG8_STAGE(bufoff, gbase, voff) do { _Pragma("unroll") for (int _i = 0; _i < 2; ++_i) \
;         __builtin_amdgcn_global_load_lds((const unsigned*)((const char*)(gbase) + (voff)[_i]), (PG8_LAS unsigned*)(lds + (bufoff) + ldsw + _i * 8192), 16, 0, 0); } while (0)
; #define PG8_WAIT_V(n) asm volatile("s_waitcnt vmcnt(" #n ")" ::: "memory")
; #define PG8_WAIT_L(n) asm volatile("s_waitcnt lgkmcnt(" #n ")" ::: "memory")
; #define PG8_BAR __builtin_amdgcn_s_barrier()
; #define PG8_SCHED __builtin_amdgcn_sched_barrier(0)
; template <class Epi, class Sched, bool ALIGN_EPI = true, bool F8 = false>
; __device__ __forceinline__ void gemm_phase(PG8_LAS unsigned char* lds, const Sched& S, const Epi& E) {
;     ...
;             PG8_LDB(B0, 1, 0); PG8_LDB(B1, 1, 1); PG8_SCHED; PG8_LDA(At, 1, 0); PG8_STAGE(PG8_SA(0, 1), a2, vA2[1]);
;             PG8_WAIT_V(8); PG8_WAIT_L(0); PG8_BAR; PG8_MMA(0, 0, At, B0); PG8_MMA(0, 1, At, B1); PG8_BAR; PG8_SCHED;
;             PG8_LDA(At, 1, 1); PG8_STAGE(PG8_SB(1, 0), b3, voffB[0]); PG8_STAGE(PG8_SB(1, 1), b3, voffB[1]); PG8_STAGE(PG8_SA(1, 0), a3, vA2[0]);
;             PG8_WAIT_V(8); PG8_WAIT_L(0); PG8_BAR; PG8_MMA(1, 0, At, B0); PG8_MMA(1, 1, At, B1); PG8_BAR; PG8_SCHED;
;         }
	s_add_i32 s66, 0, 0x18000
	s_add_i32 s67, 0, 0x1c000
	v_add_u32_e32 v14, s66, v189
	v_add_u32_e32 v30, s67, v189
	ds_read_b128 v[2:5], v14
	ds_read_b128 v[6:9], v14 offset:1024
	ds_read_b128 v[10:13], v14 offset:2048
	ds_read_b128 v[14:17], v14 offset:3072
	ds_read_b128 v[18:21], v30
	ds_read_b128 v[22:25], v30 offset:1024
	ds_read_b128 v[26:29], v30 offset:2048
	ds_read_b128 v[30:33], v30 offset:3072
	s_mov_b32 m0, s50
	v_lshl_add_u64 v[228:229], s[42:43], 0, v[172:173]
	ds_read_b128 v[196:199], v193 offset:32768
	ds_read_b128 v[200:203], v193 offset:33792
	ds_read_b128 v[204:207], v193 offset:34816
	ds_read_b128 v[208:211], v193 offset:35840
	ds_read_b128 v[212:215], v193 offset:36864
	ds_read_b128 v[216:219], v193 offset:37888
	ds_read_b128 v[220:223], v193 offset:38912
	ds_read_b128 v[224:227], v193 offset:39936
	global_load_lds_dwordx4 v[228:229], off
	v_lshl_add_u64 v[228:229], s[42:43], 0, v[174:175]
	s_mov_b32 m0, s51
	s_nop 0
	global_load_lds_dwordx4 v[228:229], off
	s_waitcnt vmcnt(8)
	s_waitcnt lgkmcnt(0)
	s_setprio 1
	v_mfma_scale_f32_16x16x128_f8f6f4 v[158:161], v[2:9], v[196:203], v[158:161], v194, v194 op_sel_hi:[0,0,0]
	v_mfma_scale_f32_16x16x128_f8f6f4 v[154:157], v[10:17], v[196:203], v[154:157], v194, v194 op_sel_hi:[0,0,0]
	v_mfma_scale_f32_16x16x128_f8f6f4 v[150:153], v[2:9], v[204:211], v[150:153], v194, v194 op_sel_hi:[0,0,0]
	v_mfma_scale_f32_16x16x128_f8f6f4 v[146:149], v[10:17], v[204:211], v[146:149], v194, v194 op_sel_hi:[0,0,0]
	v_mfma_scale_f32_16x16x128_f8f6f4 v[130:133], v[2:9], v[212:219], v[130:133], v194, v194 op_sel_hi:[0,0,0]
	v_mfma_scale_f32_16x16x128_f8f6f4 v[122:125], v[10:17], v[212:219], v[122:125], v194, v194 op_sel_hi:[0,0,0]
	v_mfma_scale_f32_16x16x128_f8f6f4 v[114:117], v[2:9], v[220:227], v[114:117], v194, v194 op_sel_hi:[0,0,0]
	v_mfma_scale_f32_16x16x128_f8f6f4 v[106:109], v[10:17], v[220:227], v[106:109], v194, v194 op_sel_hi:[0,0,0]
	s_nop 3
	s_setprio 0
	s_setprio 1
	v_mfma_scale_f32_16x16x128_f8f6f4 v[142:145], v[18:25], v[196:203], v[142:145], v194, v194 op_sel_hi:[0,0,0]
	v_mfma_scale_f32_16x16x128_f8f6f4 v[138:141], v[26:33], v[196:203], v[138:141], v194, v194 op_sel_hi:[0,0,0]
	v_mfma_scale_f32_16x16x128_f8f6f4 v[134:137], v[18:25], v[204:211], v[134:137], v194, v194 op_sel_hi:[0,0,0]
	v_mfma_scale_f32_16x16x128_f8f6f4 v[126:129], v[26:33], v[204:211], v[126:129], v194, v194 op_sel_hi:[0,0,0]
	v_mfma_scale_f32_16x16x128_f8f6f4 v[118:121], v[18:25], v[212:219], v[118:121], v194, v194 op_sel_hi:[0,0,0]
	v_mfma_scale_f32_16x16x128_f8f6f4 v[110:113], v[26:33], v[212:219], v[110:113], v194, v194 op_sel_hi:[0,0,0]
	v_mfma_scale_f32_16x16x128_f8f6f4 v[102:105], v[18:25], v[220:227], v[102:105], v194, v194 op_sel_hi:[0,0,0]
	v_mfma_scale_f32_16x16x128_f8f6f4 v[98:101], v[26:33], v[220:227], v[98:101], v194, v194 op_sel_hi:[0,0,0]
	s_setprio 0
	s_barrier
	s_add_u32 s40, s40, 0x8000
	s_addc_u32 s41, s41, 0
	s_add_i32 s42, s66, s48
	v_lshl_add_u64 v[228:229], s[40:41], 0, v[162:163]
	s_mov_b32 m0, s42
	ds_read_b128 v[196:199], v193 offset:49152
	ds_read_b128 v[200:203], v193 offset:50176
	ds_read_b128 v[204:207], v193 offset:51200
	ds_read_b128 v[208:211], v193 offset:52224
	ds_read_b128 v[212:215], v193 offset:53248
	ds_read_b128 v[216:219], v193 offset:54272
	ds_read_b128 v[220:223], v193 offset:55296
	ds_read_b128 v[224:227], v193 offset:56320
	global_load_lds_dwordx4 v[228:229], off
	v_lshl_add_u64 v[228:229], s[40:41], 0, v[164:165]
	s_add_i32 m0, s42, 0x2000
	s_add_i32 s42, s67, s48
	global_load_lds_dwordx4 v[228:229], off
	v_lshl_add_u64 v[228:229], s[40:41], 0, v[176:177]
	s_mov_b32 m0, s42
	s_nop 0
	global_load_lds_dwordx4 v[228:229], off
	v_lshl_add_u64 v[228:229], s[40:41], 0, v[178:179]
	s_add_i32 m0, s42, 0x2000
	s_nop 0
	global_load_lds_dwordx4 v[228:229], off
	v_lshl_add_u64 v[228:229], s[30:31], 0, v[166:167]
	s_mov_b32 m0, s53
	s_nop 0
	global_load_lds_dwordx4 v[228:229], off
	v_lshl_add_u64 v[228:229], s[30:31], 0, v[168:169]
	s_mov_b32 m0, s58
	s_nop 0
	global_load_lds_dwordx4 v[228:229], off
	s_waitcnt vmcnt(8)
	s_waitcnt lgkmcnt(0)
	s_setprio 1
	v_mfma_scale_f32_16x16x128_f8f6f4 v[94:97], v[2:9], v[196:203], v[94:97], v194, v194 op_sel_hi:[0,0,0]
	v_mfma_scale_f32_16x16x128_f8f6f4 v[90:93], v[10:17], v[196:203], v[90:93], v194, v194 op_sel_hi:[0,0,0]
	v_mfma_scale_f32_16x16x128_f8f6f4 v[82:85], v[2:9], v[204:211], v[82:85], v194, v194 op_sel_hi:[0,0,0]
	v_mfma_scale_f32_16x16x128_f8f6f4 v[74:77], v[10:17], v[204:211], v[74:77], v194, v194 op_sel_hi:[0,0,0]
	v_mfma_scale_f32_16x16x128_f8f6f4 v[66:69], v[2:9], v[212:219], v[66:69], v194, v194 op_sel_hi:[0,0,0]
	v_mfma_scale_f32_16x16x128_f8f6f4 v[58:61], v[10:17], v[212:219], v[58:61], v194, v194 op_sel_hi:[0,0,0]
	v_mfma_scale_f32_16x16x128_f8f6f4 v[50:53], v[2:9], v[220:227], v[50:53], v194, v194 op_sel_hi:[0,0,0]
	v_mfma_scale_f32_16x16x128_f8f6f4 v[42:45], v[10:17], v[220:227], v[42:45], v194, v194 op_sel_hi:[0,0,0]
	s_nop 3
	s_setprio 0
	s_setprio 1
	v_mfma_scale_f32_16x16x128_f8f6f4 v[86:89], v[18:25], v[196:203], v[86:89], v194, v194 op_sel_hi:[0,0,0]
	v_mfma_scale_f32_16x16x128_f8f6f4 v[78:81], v[26:33], v[196:203], v[78:81], v194, v194 op_sel_hi:[0,0,0]
	v_mfma_scale_f32_16x16x128_f8f6f4 v[70:73], v[18:25], v[204:211], v[70:73], v194, v194 op_sel_hi:[0,0,0]
	v_mfma_scale_f32_16x16x128_f8f6f4 v[62:65], v[26:33], v[204:211], v[62:65], v194, v194 op_sel_hi:[0,0,0]
	v_mfma_scale_f32_16x16x128_f8f6f4 v[54:57], v[18:25], v[212:219], v[54:57], v194, v194 op_sel_hi:[0,0,0]
	v_mfma_scale_f32_16x16x128_f8f6f4 v[46:49], v[26:33], v[212:219], v[46:49], v194, v194 op_sel_hi:[0,0,0]
	v_mfma_scale_f32_16x16x128_f8f6f4 v[38:41], v[18:25], v[220:227], v[38:41], v194, v194 op_sel_hi:[0,0,0]
	v_mfma_scale_f32_16x16x128_f8f6f4 v[34:37], v[26:33], v[220:227], v[34:37], v194, v194 op_sel_hi:[0,0,0]
	s_setprio 0
	s_barrier
	s_add_i32 s65, s65, 2
	s_add_u32 s19, s19, 0x10000
	s_addc_u32 s21, s21, 0
	s_add_u32 s28, s28, 0x10000
	s_addc_u32 s29, s29, 0
	s_cmp_gt_u32 s65, 13
	s_cbranch_scc0 .LBB0_911
	s_branch .Lfx_26630

; #define PG8_STAGE(bufoff, gbase, voff) do { _Pragma("unroll") for (int _i = 0; _i < 2; ++_i) \
;         __builtin_amdgcn_global_load_lds((const unsigned*)((const char*)(gbase) + (voff)[_i]), (PG8_LAS unsigned*)(lds + (bufoff) + ldsw + _i * 8192), 16, 0, 0); } while (0)
; #define PG8_WAIT_V(n) asm volatile("s_waitcnt vmcnt(" #n ")" ::: "memory")
; #define PG8_WAIT_L(n) asm volatile("s_waitcnt lgkmcnt(" #n ")" ::: "memory")
; #define PG8_BAR __builtin_amdgcn_s_barrier()
; #define PG8_SCHED __builtin_amdgcn_sched_barrier(0)
; template <class Epi, class Sched, bool ALIGN_EPI = true, bool F8 = false>
; __device__ __forceinline__ void gemm_phase(PG8_LAS unsigned char* lds, const Sched& S, const Epi& E) {
;     ...
;             PG8_LDB(B0, 0, 0); PG8_LDB(B1, 0, 1); PG8_SCHED; PG8_LDA(At, 0, 0); PG8_STAGE(PG8_SA(1, 1), a1, voffA[1]);
;             PG8_WAIT_V(8); PG8_WAIT_L(0); PG8_BAR; PG8_MMA(0, 0, At, B0); PG8_MMA(0, 1, At, B1); PG8_BAR; PG8_SCHED;
;             PG8_LDA(At, 0, 1); PG8_STAGE(PG8_SB(0, 0), b2, voffB[0]); PG8_STAGE(PG8_SB(0, 1), b2, voffB[1]); PG8_STAGE(PG8_SA(0, 0), a2, vA2[0]);
;             PG8_WAIT_V(8); PG8_WAIT_L(0); PG8_BAR; PG8_MMA(1, 0, At, B0); PG8_MMA(1, 1, At, B1); PG8_BAR; PG8_SCHED;
;             PG8_LDB(B0, 1, 0); PG8_LDB(B1, 1, 1); PG8_SCHED; PG8_LDA(At, 1, 0); PG8_STAGE(PG8_SA(0, 1), a2, vA2[1]);
;             PG8_WAIT_V(8); PG8_WAIT_L(0); PG8_BAR; PG8_MMA(0, 0, At, B0); PG8_MMA(0, 1, At, B1); PG8_BAR; PG8_SCHED;
.Lh1e_26630:
.Lpk1_911:
	ds_read_b128 v[18:21], v191
	ds_read_b128 v[22:25], v191 offset:1024
	ds_read_b128 v[26:29], v191 offset:2048
	ds_read_b128 v[30:33], v191 offset:3072
	ds_read_b128 v[2:5], v192
	ds_read_b128 v[6:9], v192 offset:1024
	ds_read_b128 v[10:13], v192 offset:2048
	ds_read_b128 v[14:17], v192 offset:3072
	s_add_u32 s30, s28, 0x8000
	s_addc_u32 s31, s29, 0
	s_cmp_eq_u32 s65, 12
	s_cselect_b32 s42, s22, s30
	s_cselect_b32 s43, s23, s31
	s_cselect_b32 s40, s24, s19
	s_cselect_b32 s41, s25, s21
	s_add_u32 s30, s42, 0x8000
	s_addc_u32 s31, s43, 0
	v_lshl_add_u64 v[228:229], s[28:29], 0, v[182:183]
	s_add_i32 m0, s27, 0xc000
	ds_read_b128 v[196:199], v193
	ds_read_b128 v[200:203], v193 offset:1024
	ds_read_b128 v[204:207], v193 offset:2048
	ds_read_b128 v[208:211], v193 offset:3072
	ds_read_b128 v[212:215], v193 offset:4096
	ds_read_b128 v[216:219], v193 offset:5120
	ds_read_b128 v[220:223], v193 offset:6144
	ds_read_b128 v[224:227], v193 offset:7168
	global_load_lds_dwordx4 v[228:229], off
	v_lshl_add_u64 v[228:229], s[28:29], 0, v[180:181]
	s_add_i32 m0, s27, 0xe000
	s_nop 0
	global_load_lds_dwordx4 v[228:229], off
	s_waitcnt vmcnt(16)
	s_waitcnt lgkmcnt(0)
	s_barrier
	s_setprio 2
	v_mfma_scale_f32_16x16x128_f8f6f4 v[158:161], v[18:25], v[196:203], 0, v194, v194 op_sel_hi:[0,0,0]
	v_mfma_scale_f32_16x16x128_f8f6f4 v[154:157], v[26:33], v[196:203], 0, v194, v194 op_sel_hi:[0,0,0]
	v_mfma_scale_f32_16x16x128_f8f6f4 v[150:153], v[18:25], v[204:211], 0, v194, v194 op_sel_hi:[0,0,0]
	v_mfma_scale_f32_16x16x128_f8f6f4 v[146:149], v[26:33], v[204:211], 0, v194, v194 op_sel_hi:[0,0,0]
	v_mfma_scale_f32_16x16x128_f8f6f4 v[130:133], v[18:25], v[212:219], 0, v194, v194 op_sel_hi:[0,0,0]
	v_mfma_scale_f32_16x16x128_f8f6f4 v[122:125], v[26:33], v[212:219], 0, v194, v194 op_sel_hi:[0,0,0]
	v_mfma_scale_f32_16x16x128_f8f6f4 v[114:117], v[18:25], v[220:227], 0, v194, v194 op_sel_hi:[0,0,0]
	v_mfma_scale_f32_16x16x128_f8f6f4 v[106:109], v[26:33], v[220:227], 0, v194, v194 op_sel_hi:[0,0,0]
	s_nop 3
	s_setprio 0
	s_setprio 2
	v_mfma_scale_f32_16x16x128_f8f6f4 v[142:145], v[2:9], v[196:203], 0, v194, v194 op_sel_hi:[0,0,0]
	v_mfma_scale_f32_16x16x128_f8f6f4 v[138:141], v[10:17], v[196:203], 0, v194, v194 op_sel_hi:[0,0,0]
	v_mfma_scale_f32_16x16x128_f8f6f4 v[134:137], v[2:9], v[204:211], 0, v194, v194 op_sel_hi:[0,0,0]
	v_mfma_scale_f32_16x16x128_f8f6f4 v[126:129], v[10:17], v[204:211], 0, v194, v194 op_sel_hi:[0,0,0]
	v_mfma_scale_f32_16x16x128_f8f6f4 v[118:121], v[2:9], v[212:219], 0, v194, v194 op_sel_hi:[0,0,0]
	v_mfma_scale_f32_16x16x128_f8f6f4 v[110:113], v[10:17], v[212:219], 0, v194, v194 op_sel_hi:[0,0,0]
	v_mfma_scale_f32_16x16x128_f8f6f4 v[102:105], v[2:9], v[220:227], 0, v194, v194 op_sel_hi:[0,0,0]
	v_mfma_scale_f32_16x16x128_f8f6f4 v[98:101], v[10:17], v[220:227], 0, v194, v194 op_sel_hi:[0,0,0]
	s_setprio 0
	s_add_i32 s66, s60, s48
	v_lshl_add_u64 v[228:229], s[40:41], 0, v[162:163]
	s_mov_b32 m0, s66
	ds_read_b128 v[196:199], v193 offset:16384
	ds_read_b128 v[200:203], v193 offset:17408
	ds_read_b128 v[204:207], v193 offset:18432
	ds_read_b128 v[208:211], v193 offset:19456
	ds_read_b128 v[212:215], v193 offset:20480
	ds_read_b128 v[216:219], v193 offset:21504
	ds_read_b128 v[220:223], v193 offset:22528
	ds_read_b128 v[224:227], v193 offset:23552
	global_load_lds_dwordx4 v[228:229], off
	v_lshl_add_u64 v[230:231], s[40:41], 0, v[164:165]
	s_add_i32 m0, s66, 0x2000
	s_add_i32 s66, s61, s48
	global_load_lds_dwordx4 v[230:231], off
	v_lshl_add_u64 v[228:229], v[228:229], 0, s[6:7]
	s_mov_b32 m0, s66
	s_nop 0
	global_load_lds_dwordx4 v[228:229], off
	v_lshl_add_u64 v[228:229], v[230:231], 0, s[6:7]
	s_add_i32 m0, s66, 0x2000
	s_nop 0
	global_load_lds_dwordx4 v[228:229], off
	v_lshl_add_u64 v[228:229], s[42:43], 0, v[166:167]
	s_mov_b32 m0, s27
	s_nop 0
	global_load_lds_dwordx4 v[228:229], off
	v_lshl_add_u64 v[228:229], s[42:43], 0, v[168:169]
	s_mov_b32 m0, s49
	s_nop 0
	global_load_lds_dwordx4 v[228:229], off
	s_waitcnt vmcnt(16)
	s_waitcnt lgkmcnt(0)
	s_barrier
	s_setprio 2
	v_mfma_scale_f32_16x16x128_f8f6f4 v[94:97], v[18:25], v[196:203], 0, v194, v194 op_sel_hi:[0,0,0]
	v_mfma_scale_f32_16x16x128_f8f6f4 v[90:93], v[26:33], v[196:203], 0, v194, v194 op_sel_hi:[0,0,0]
	v_mfma_scale_f32_16x16x128_f8f6f4 v[82:85], v[18:25], v[204:211], 0, v194, v194 op_sel_hi:[0,0,0]
	v_mfma_scale_f32_16x16x128_f8f6f4 v[74:77], v[26:33], v[204:211], 0, v194, v194 op_sel_hi:[0,0,0]
	v_mfma_scale_f32_16x16x128_f8f6f4 v[66:69], v[18:25], v[212:219], 0, v194, v194 op_sel_hi:[0,0,0]
	v_mfma_scale_f32_16x16x128_f8f6f4 v[58:61], v[26:33], v[212:219], 0, v194, v194 op_sel_hi:[0,0,0]
	v_mfma_scale_f32_16x16x128_f8f6f4 v[50:53], v[18:25], v[220:227], 0, v194, v194 op_sel_hi:[0,0,0]
	v_mfma_scale_f32_16x16x128_f8f6f4 v[42:45], v[26:33], v[220:227], 0, v194, v194 op_sel_hi:[0,0,0]
	s_nop 3
	s_setprio 0
	s_setprio 2
	v_mfma_scale_f32_16x16x128_f8f6f4 v[86:89], v[2:9], v[196:203], 0, v194, v194 op_sel_hi:[0,0,0]
	v_mfma_scale_f32_16x16x128_f8f6f4 v[78:81], v[10:17], v[196:203], 0, v194, v194 op_sel_hi:[0,0,0]
	v_mfma_scale_f32_16x16x128_f8f6f4 v[70:73], v[2:9], v[204:211], 0, v194, v194 op_sel_hi:[0,0,0]
	v_mfma_scale_f32_16x16x128_f8f6f4 v[62:65], v[10:17], v[204:211], 0, v194, v194 op_sel_hi:[0,0,0]
	v_mfma_scale_f32_16x16x128_f8f6f4 v[54:57], v[2:9], v[212:219], 0, v194, v194 op_sel_hi:[0,0,0]
	v_mfma_scale_f32_16x16x128_f8f6f4 v[46:49], v[10:17], v[212:219], 0, v194, v194 op_sel_hi:[0,0,0]
	v_mfma_scale_f32_16x16x128_f8f6f4 v[38:41], v[2:9], v[220:227], 0, v194, v194 op_sel_hi:[0,0,0]
	v_mfma_scale_f32_16x16x128_f8f6f4 v[34:37], v[10:17], v[220:227], 0, v194, v194 op_sel_hi:[0,0,0]
	s_setprio 0
	s_add_i32 s66, 0, 0x18000
	s_add_i32 s67, 0, 0x1c000
	v_add_u32_e32 v14, s66, v189
	v_add_u32_e32 v30, s67, v189
	ds_read_b128 v[2:5], v14
	ds_read_b128 v[6:9], v14 offset:1024
	ds_read_b128 v[10:13], v14 offset:2048
	ds_read_b128 v[14:17], v14 offset:3072
	ds_read_b128 v[18:21], v30
	ds_read_b128 v[22:25], v30 offset:1024
	ds_read_b128 v[26:29], v30 offset:2048
	ds_read_b128 v[30:33], v30 offset:3072
	s_mov_b32 m0, s50
	v_lshl_add_u64 v[228:229], s[42:43], 0, v[172:173]
	ds_read_b128 v[196:199], v193 offset:32768
	ds_read_b128 v[200:203], v193 offset:33792
	ds_read_b128 v[204:207], v193 offset:34816
	ds_read_b128 v[208:211], v193 offset:35840
	ds_read_b128 v[212:215], v193 offset:36864
	ds_read_b128 v[216:219], v193 offset:37888
	ds_read_b128 v[220:223], v193 offset:38912
	ds_read_b128 v[224:227], v193 offset:39936
	global_load_lds_dwordx4 v[228:229], off
	v_lshl_add_u64 v[228:229], s[42:43], 0, v[174:175]
	s_mov_b32 m0, s51
	s_nop 0
	global_load_lds_dwordx4 v[228:229], off
	s_waitcnt vmcnt(8)
	s_waitcnt lgkmcnt(0)
	s_barrier
; #define PG8_STAGE(bufoff, gbase, voff) do { _Pragma("unroll") for (int _i = 0; _i < 2; ++_i) \
;         __builtin_amdgcn_global_load_lds((const unsigned*)((const char*)(gbase) + (voff)[_i]), (PG8_LAS unsigned*)(lds + (bufoff) + ldsw + _i * 8192), 16, 0, 0); } while (0)
; #define PG8_WAIT_V(n) asm volatile("s_waitcnt vmcnt(" #n ")" ::: "memory")
; #define PG8_WAIT_L(n) asm volatile("s_waitcnt lgkmcnt(" #n ")" ::: "memory")
; #define PG8_BAR __builtin_amdgcn_s_barrier()
; #define PG8_SCHED __builtin_amdgcn_sched_barrier(0)
; template <class Epi, class Sched, bool ALIGN_EPI = true, bool F8 = false>
; __device__ __forceinline__ void gemm_phase(PG8_LAS unsigned char* lds, const Sched& S, const Epi& E) {
;     ...
;             PG8_WAIT_V(8); PG8_WAIT_L(0); PG8_BAR; PG8_MMA(0, 0, At, B0); PG8_MMA(0, 1, At, B1); PG8_BAR; PG8_SCHED;
;             PG8_LDA(At, 1, 1); PG8_STAGE(PG8_SB(1, 0), b3, voffB[0]); PG8_STAGE(PG8_SB(1, 1), b3, voffB[1]); PG8_STAGE(PG8_SA(1, 0), a3, vA2[0]);
;             PG8_WAIT_V(8); PG8_WAIT_L(0); PG8_BAR; PG8_MMA(1, 0, At, B0); PG8_MMA(1, 1, At, B1); PG8_BAR; PG8_SCHED;
;         }
	s_setprio 2
	v_mfma_scale_f32_16x16x128_f8f6f4 v[158:161], v[2:9], v[196:203], v[158:161], v194, v194 op_sel_hi:[0,0,0]
	v_mfma_scale_f32_16x16x128_f8f6f4 v[154:157], v[10:17], v[196:203], v[154:157], v194, v194 op_sel_hi:[0,0,0]
	v_mfma_scale_f32_16x16x128_f8f6f4 v[150:153], v[2:9], v[204:211], v[150:153], v194, v194 op_sel_hi:[0,0,0]
	v_mfma_scale_f32_16x16x128_f8f6f4 v[146:149], v[10:17], v[204:211], v[146:149], v194, v194 op_sel_hi:[0,0,0]
	v_mfma_scale_f32_16x16x128_f8f6f4 v[130:133], v[2:9], v[212:219], v[130:133], v194, v194 op_sel_hi:[0,0,0]
	v_mfma_scale_f32_16x16x128_f8f6f4 v[122:125], v[10:17], v[212:219], v[122:125], v194, v194 op_sel_hi:[0,0,0]
	v_mfma_scale_f32_16x16x128_f8f6f4 v[114:117], v[2:9], v[220:227], v[114:117], v194, v194 op_sel_hi:[0,0,0]
	v_mfma_scale_f32_16x16x128_f8f6f4 v[106:109], v[10:17], v[220:227], v[106:109], v194, v194 op_sel_hi:[0,0,0]
	s_nop 3
	s_setprio 0
	s_setprio 2
	v_mfma_scale_f32_16x16x128_f8f6f4 v[142:145], v[18:25], v[196:203], v[142:145], v194, v194 op_sel_hi:[0,0,0]
	v_mfma_scale_f32_16x16x128_f8f6f4 v[138:141], v[26:33], v[196:203], v[138:141], v194, v194 op_sel_hi:[0,0,0]
	v_mfma_scale_f32_16x16x128_f8f6f4 v[134:137], v[18:25], v[204:211], v[134:137], v194, v194 op_sel_hi:[0,0,0]
	v_mfma_scale_f32_16x16x128_f8f6f4 v[126:129], v[26:33], v[204:211], v[126:129], v194, v194 op_sel_hi:[0,0,0]
	v_mfma_scale_f32_16x16x128_f8f6f4 v[118:121], v[18:25], v[212:219], v[118:121], v194, v194 op_sel_hi:[0,0,0]
	v_mfma_scale_f32_16x16x128_f8f6f4 v[110:113], v[26:33], v[212:219], v[110:113], v194, v194 op_sel_hi:[0,0,0]
	v_mfma_scale_f32_16x16x128_f8f6f4 v[102:105], v[18:25], v[220:227], v[102:105], v194, v194 op_sel_hi:[0,0,0]
	v_mfma_scale_f32_16x16x128_f8f6f4 v[98:101], v[26:33], v[220:227], v[98:101], v194, v194 op_sel_hi:[0,0,0]
	s_setprio 0
	s_add_u32 s40, s40, 0x8000
	s_addc_u32 s41, s41, 0
	s_add_i32 s42, s66, s48
	v_lshl_add_u64 v[228:229], s[40:41], 0, v[162:163]
	s_mov_b32 m0, s42
	ds_read_b128 v[196:199], v193 offset:49152
	ds_read_b128 v[200:203], v193 offset:50176
	ds_read_b128 v[204:207], v193 offset:51200
	ds_read_b128 v[208:211], v193 offset:52224
	ds_read_b128 v[212:215], v193 offset:53248
	ds_read_b128 v[216:219], v193 offset:54272
	ds_read_b128 v[220:223], v193 offset:55296
	ds_read_b128 v[224:227], v193 offset:56320
	global_load_lds_dwordx4 v[228:229], off
	v_lshl_add_u64 v[228:229], s[40:41], 0, v[164:165]
	s_add_i32 m0, s42, 0x2000
	s_add_i32 s42, s67, s48
	global_load_lds_dwordx4 v[228:229], off
	v_lshl_add_u64 v[228:229], s[40:41], 0, v[176:177]
	s_mov_b32 m0, s42
	s_nop 0
	global_load_lds_dwordx4 v[228:229], off
	v_lshl_add_u64 v[228:229], s[40:41], 0, v[178:179]
	s_add_i32 m0, s42, 0x2000
	s_nop 0
	global_load_lds_dwordx4 v[228:229], off
	v_lshl_add_u64 v[228:229], s[30:31], 0, v[166:167]
	s_mov_b32 m0, s53
	s_nop 0
	global_load_lds_dwordx4 v[228:229], off
	v_lshl_add_u64 v[228:229], s[30:31], 0, v[168:169]
	s_mov_b32 m0, s58
	s_nop 0
	global_load_lds_dwordx4 v[228:229], off
	s_waitcnt vmcnt(8)
	s_waitcnt lgkmcnt(0)
	s_barrier
	s_setprio 2
	v_mfma_scale_f32_16x16x128_f8f6f4 v[94:97], v[2:9], v[196:203], v[94:97], v194, v194 op_sel_hi:[0,0,0]
	v_mfma_scale_f32_16x16x128_f8f6f4 v[90:93], v[10:17], v[196:203], v[90:93], v194, v194 op_sel_hi:[0,0,0]
	v_mfma_scale_f32_16x16x128_f8f6f4 v[82:85], v[2:9], v[204:211], v[82:85], v194, v194 op_sel_hi:[0,0,0]
	v_mfma_scale_f32_16x16x128_f8f6f4 v[74:77], v[10:17], v[204:211], v[74:77], v194, v194 op_sel_hi:[0,0,0]
	v_mfma_scale_f32_16x16x128_f8f6f4 v[66:69], v[2:9], v[212:219], v[66:69], v194, v194 op_sel_hi:[0,0,0]
	v_mfma_scale_f32_16x16x128_f8f6f4 v[58:61], v[10:17], v[212:219], v[58:61], v194, v194 op_sel_hi:[0,0,0]
	v_mfma_scale_f32_16x16x128_f8f6f4 v[50:53], v[2:9], v[220:227], v[50:53], v194, v194 op_sel_hi:[0,0,0]
	v_mfma_scale_f32_16x16x128_f8f6f4 v[42:45], v[10:17], v[220:227], v[42:45], v194, v194 op_sel_hi:[0,0,0]
	s_nop 3
	s_setprio 0
	s_setprio 2
	v_mfma_scale_f32_16x16x128_f8f6f4 v[86:89], v[18:25], v[196:203], v[86:89], v194, v194 op_sel_hi:[0,0,0]
	v_mfma_scale_f32_16x16x128_f8f6f4 v[78:81], v[26:33], v[196:203], v[78:81], v194, v194 op_sel_hi:[0,0,0]
	v_mfma_scale_f32_16x16x128_f8f6f4 v[70:73], v[18:25], v[204:211], v[70:73], v194, v194 op_sel_hi:[0,0,0]
	v_mfma_scale_f32_16x16x128_f8f6f4 v[62:65], v[26:33], v[204:211], v[62:65], v194, v194 op_sel_hi:[0,0,0]
	v_mfma_scale_f32_16x16x128_f8f6f4 v[54:57], v[18:25], v[212:219], v[54:57], v194, v194 op_sel_hi:[0,0,0]
	v_mfma_scale_f32_16x16x128_f8f6f4 v[46:49], v[26:33], v[212:219], v[46:49], v194, v194 op_sel_hi:[0,0,0]
	v_mfma_scale_f32_16x16x128_f8f6f4 v[38:41], v[18:25], v[220:227], v[38:41], v194, v194 op_sel_hi:[0,0,0]
	v_mfma_scale_f32_16x16x128_f8f6f4 v[34:37], v[26:33], v[220:227], v[34:37], v194, v194 op_sel_hi:[0,0,0]
	s_setprio 0
	s_add_i32 s65, s65, 2
	s_add_u32 s19, s19, 0x10000
	s_addc_u32 s21, s21, 0
	s_add_u32 s28, s28, 0x10000
	s_addc_u32 s29, s29, 0
	s_cmp_gt_u32 s65, 13
	s_cbranch_scc0 .Lh1_911
	s_branch .Lfx_26630
